# baseline (speedup 1.0000x reference)
_Z13logits_kernelPKDv8_DF16bS1_PKfS3_PDv2_fS5_Pf:
	s_load_dwordx4 s[4:7], s[0:1], 0x0
	s_load_dwordx4 s[12:15], s[0:1], 0x10
	s_lshl_b32 s3, s2, 1
	s_and_b32 s3, s3, 14
	s_ashr_i32 s8, s2, 7
	s_bfe_u32 s10, s2, 0x40003
	s_add_i32 s3, s3, s8
	v_lshrrev_b32_e32 v1, 6, v0
	v_and_b32_e32 v2, 63, v0
	s_movk_i32 s11, 0x3000
	v_lshlrev_b32_e32 v2, 4, v2
	v_and_b32_e32 v5, 31, v0
	v_mad_u32_u24 v2, v1, s11, v2
	v_lshlrev_b32_e32 v5, 2, v5
	s_lshl_b32 s9, s3, 9
	v_add_u32_e32 v3, 0x1000, v2
	v_add_u32_e32 v4, 0x2000, v2
	v_add_u32_e32 v5, s9, v5
	s_mul_i32 s8, s10, 0xc000
	s_mul_i32 s9, s3, 0x30000
	s_waitcnt lgkmcnt(0)
	s_load_dword s22, s[14:15], 0x0
	global_load_dword v248, v5, s[12:13]
	global_load_dword v249, v5, s[12:13] offset:128
	global_load_dword v250, v5, s[12:13] offset:256
	global_load_dword v251, v5, s[12:13] offset:384
	s_add_u32 s4, s4, s8
	s_addc_u32 s5, s5, 0
	s_add_u32 s6, s6, s9
	s_addc_u32 s7, s7, 0
	s_add_u32 s16, s6, 0xc000
	s_addc_u32 s17, s7, 0
	s_add_u32 s18, s6, 0x18000
	s_addc_u32 s19, s7, 0
	s_add_u32 s20, s6, 0x24000
	s_addc_u32 s21, s7, 0
	global_load_dwordx4 v[8:11], v2, s[4:5] sc1
	global_load_dwordx4 v[56:59], v2, s[6:7] sc1
	global_load_dwordx4 v[104:107], v2, s[16:17] sc1
	global_load_dwordx4 v[152:155], v2, s[18:19] sc1
	global_load_dwordx4 v[200:203], v2, s[20:21] sc1
	global_load_dwordx4 v[12:15], v2, s[4:5] offset:1024 sc1
	global_load_dwordx4 v[60:63], v2, s[6:7] offset:1024 sc1
	global_load_dwordx4 v[108:111], v2, s[16:17] offset:1024 sc1
	global_load_dwordx4 v[156:159], v2, s[18:19] offset:1024 sc1
	global_load_dwordx4 v[204:207], v2, s[20:21] offset:1024 sc1
	global_load_dwordx4 v[16:19], v2, s[4:5] offset:2048 sc1
	global_load_dwordx4 v[64:67], v2, s[6:7] offset:2048 sc1
	global_load_dwordx4 v[112:115], v2, s[16:17] offset:2048 sc1
	global_load_dwordx4 v[160:163], v2, s[18:19] offset:2048 sc1
	global_load_dwordx4 v[208:211], v2, s[20:21] offset:2048 sc1
	global_load_dwordx4 v[20:23], v2, s[4:5] offset:3072 sc1
	global_load_dwordx4 v[68:71], v2, s[6:7] offset:3072 sc1
	global_load_dwordx4 v[116:119], v2, s[16:17] offset:3072 sc1
	global_load_dwordx4 v[164:167], v2, s[18:19] offset:3072 sc1
	global_load_dwordx4 v[212:215], v2, s[20:21] offset:3072 sc1
	global_load_dwordx4 v[24:27], v3, s[4:5] sc1
	global_load_dwordx4 v[72:75], v3, s[6:7] sc1
	global_load_dwordx4 v[120:123], v3, s[16:17] sc1
	global_load_dwordx4 v[168:171], v3, s[18:19] sc1
	global_load_dwordx4 v[216:219], v3, s[20:21] sc1
	global_load_dwordx4 v[28:31], v3, s[4:5] offset:1024 sc1
	global_load_dwordx4 v[76:79], v3, s[6:7] offset:1024 sc1
	global_load_dwordx4 v[124:127], v3, s[16:17] offset:1024 sc1
	global_load_dwordx4 v[172:175], v3, s[18:19] offset:1024 sc1
	global_load_dwordx4 v[220:223], v3, s[20:21] offset:1024 sc1
	global_load_dwordx4 v[32:35], v3, s[4:5] offset:2048 sc1
	global_load_dwordx4 v[80:83], v3, s[6:7] offset:2048 sc1
	global_load_dwordx4 v[128:131], v3, s[16:17] offset:2048 sc1
	global_load_dwordx4 v[176:179], v3, s[18:19] offset:2048 sc1
	global_load_dwordx4 v[224:227], v3, s[20:21] offset:2048 sc1
	global_load_dwordx4 v[36:39], v3, s[4:5] offset:3072 sc1
	global_load_dwordx4 v[84:87], v3, s[6:7] offset:3072 sc1
	global_load_dwordx4 v[132:135], v3, s[16:17] offset:3072 sc1
	global_load_dwordx4 v[180:183], v3, s[18:19] offset:3072 sc1
	global_load_dwordx4 v[228:231], v3, s[20:21] offset:3072 sc1
	global_load_dwordx4 v[40:43], v4, s[4:5] sc1
	global_load_dwordx4 v[88:91], v4, s[6:7] sc1
	global_load_dwordx4 v[136:139], v4, s[16:17] sc1
	global_load_dwordx4 v[184:187], v4, s[18:19] sc1
	global_load_dwordx4 v[232:235], v4, s[20:21] sc1
	global_load_dwordx4 v[44:47], v4, s[4:5] offset:1024 sc1
	global_load_dwordx4 v[92:95], v4, s[6:7] offset:1024 sc1
	global_load_dwordx4 v[140:143], v4, s[16:17] offset:1024 sc1
	global_load_dwordx4 v[188:191], v4, s[18:19] offset:1024 sc1
	global_load_dwordx4 v[236:239], v4, s[20:21] offset:1024 sc1
	global_load_dwordx4 v[48:51], v4, s[4:5] offset:2048 sc1
	global_load_dwordx4 v[96:99], v4, s[6:7] offset:2048 sc1
	global_load_dwordx4 v[144:147], v4, s[16:17] offset:2048 sc1
	global_load_dwordx4 v[192:195], v4, s[18:19] offset:2048 sc1
	global_load_dwordx4 v[240:243], v4, s[20:21] offset:2048 sc1
	global_load_dwordx4 v[52:55], v4, s[4:5] offset:3072 sc1
	global_load_dwordx4 v[100:103], v4, s[6:7] offset:3072 sc1
	global_load_dwordx4 v[148:151], v4, s[16:17] offset:3072 sc1
	global_load_dwordx4 v[196:199], v4, s[18:19] offset:3072 sc1
	global_load_dwordx4 v[244:247], v4, s[20:21] offset:3072 sc1
	s_waitcnt vmcnt(58)
	v_mfma_f32_32x32x16_bf16 a[0:15], v[8:11], v[56:59], 0
	s_waitcnt vmcnt(57)
	v_mfma_f32_32x32x16_bf16 a[0:15], v[8:11], v[104:107], a[0:15]
	s_waitcnt vmcnt(56)
	v_mfma_f32_32x32x16_bf16 a[0:15], v[8:11], v[152:155], a[0:15]
	s_waitcnt vmcnt(55)
	v_mfma_f32_32x32x16_bf16 a[0:15], v[8:11], v[200:203], a[0:15]
	s_waitcnt vmcnt(53)
	v_mfma_f32_32x32x16_bf16 a[0:15], v[12:15], v[60:63], a[0:15]
	s_waitcnt vmcnt(52)
	v_mfma_f32_32x32x16_bf16 a[0:15], v[12:15], v[108:111], a[0:15]
	s_waitcnt vmcnt(51)
	v_mfma_f32_32x32x16_bf16 a[0:15], v[12:15], v[156:159], a[0:15]
	s_waitcnt vmcnt(50)
	v_mfma_f32_32x32x16_bf16 a[0:15], v[12:15], v[204:207], a[0:15]
	v_add_f32_e32 v8, 0, v248
	v_add_f32_e32 v8, v8, v249
	v_add_f32_e32 v8, v8, v250
	v_add_f32_e32 v8, v8, v251
	v_mov_b32_e32 v9, 0x3fb8aa3b
	s_waitcnt lgkmcnt(0)
	v_mul_f32_e32 v9, s22, v9
	v_exp_f32_e32 v9, v9
	v_add_f32_e32 v10, 0x2b8cbccc, v8
	v_div_scale_f32 v11, s[8:9], v10, v10, v9
	v_rcp_f32_e32 v12, v11
	v_div_scale_f32 v13, vcc, v9, v10, v9
	v_fma_f32 v14, -v11, v12, 1.0
	v_fmac_f32_e32 v12, v14, v12
	v_mul_f32_e32 v14, v13, v12
	v_fma_f32 v15, -v11, v14, v13
	v_fmac_f32_e32 v14, v15, v12
	v_fma_f32 v11, -v11, v14, v13
	v_div_fmas_f32 v11, v11, v12, v14
	v_div_fixup_f32 v9, v11, v10, v9
	v_lshlrev_b32_e32 v10, 2, v0
	v_add_u32_e32 v10, 0x4000, v10
	v_cmp_gt_u32_e32 vcc, 32, v0
	s_and_saveexec_b64 s[8:9], vcc
	ds_write2_b32 v10, v8, v9 offset0:128 offset1:160
	s_mov_b64 exec, s[8:9]
	s_waitcnt vmcnt(48)
	v_mfma_f32_32x32x16_bf16 a[0:15], v[16:19], v[64:67], a[0:15]
	s_waitcnt vmcnt(47)
	v_mfma_f32_32x32x16_bf16 a[0:15], v[16:19], v[112:115], a[0:15]
	s_waitcnt vmcnt(46)
	v_mfma_f32_32x32x16_bf16 a[0:15], v[16:19], v[160:163], a[0:15]
	s_waitcnt vmcnt(45)
	v_mfma_f32_32x32x16_bf16 a[0:15], v[16:19], v[208:211], a[0:15]
	s_waitcnt vmcnt(43)
	v_mfma_f32_32x32x16_bf16 a[0:15], v[20:23], v[68:71], a[0:15]
	s_waitcnt vmcnt(42)
	v_mfma_f32_32x32x16_bf16 a[0:15], v[20:23], v[116:119], a[0:15]
	s_waitcnt vmcnt(41)
	v_mfma_f32_32x32x16_bf16 a[0:15], v[20:23], v[164:167], a[0:15]
	s_waitcnt vmcnt(40)
	v_mfma_f32_32x32x16_bf16 a[0:15], v[20:23], v[212:215], a[0:15]
	s_waitcnt vmcnt(38)
	v_mfma_f32_32x32x16_bf16 a[0:15], v[24:27], v[72:75], a[0:15]
	s_waitcnt vmcnt(37)
	v_mfma_f32_32x32x16_bf16 a[0:15], v[24:27], v[120:123], a[0:15]
	s_waitcnt vmcnt(36)
	v_mfma_f32_32x32x16_bf16 a[0:15], v[24:27], v[168:171], a[0:15]
	s_waitcnt vmcnt(35)
	v_mfma_f32_32x32x16_bf16 a[0:15], v[24:27], v[216:219], a[0:15]
	s_waitcnt vmcnt(33)
	v_mfma_f32_32x32x16_bf16 a[0:15], v[28:31], v[76:79], a[0:15]
	s_waitcnt vmcnt(32)
	v_mfma_f32_32x32x16_bf16 a[0:15], v[28:31], v[124:127], a[0:15]
	s_waitcnt vmcnt(31)
	v_mfma_f32_32x32x16_bf16 a[0:15], v[28:31], v[172:175], a[0:15]
	s_waitcnt vmcnt(30)
	v_mfma_f32_32x32x16_bf16 a[0:15], v[28:31], v[220:223], a[0:15]
	s_waitcnt vmcnt(28)
	v_mfma_f32_32x32x16_bf16 a[0:15], v[32:35], v[80:83], a[0:15]
	s_waitcnt vmcnt(27)
	v_mfma_f32_32x32x16_bf16 a[0:15], v[32:35], v[128:131], a[0:15]
	s_waitcnt vmcnt(26)
	v_mfma_f32_32x32x16_bf16 a[0:15], v[32:35], v[176:179], a[0:15]
	s_waitcnt vmcnt(25)
	v_mfma_f32_32x32x16_bf16 a[0:15], v[32:35], v[224:227], a[0:15]
	s_waitcnt vmcnt(23)
	v_mfma_f32_32x32x16_bf16 a[0:15], v[36:39], v[84:87], a[0:15]
	s_waitcnt vmcnt(22)
	v_mfma_f32_32x32x16_bf16 a[0:15], v[36:39], v[132:135], a[0:15]
	s_waitcnt vmcnt(21)
	v_mfma_f32_32x32x16_bf16 a[0:15], v[36:39], v[180:183], a[0:15]
	s_waitcnt vmcnt(20)
	v_mfma_f32_32x32x16_bf16 a[0:15], v[36:39], v[228:231], a[0:15]
	s_waitcnt vmcnt(18)
	v_mfma_f32_32x32x16_bf16 a[0:15], v[40:43], v[88:91], a[0:15]
	s_waitcnt vmcnt(17)
	v_mfma_f32_32x32x16_bf16 a[0:15], v[40:43], v[136:139], a[0:15]
	s_waitcnt vmcnt(16)
	v_mfma_f32_32x32x16_bf16 a[0:15], v[40:43], v[184:187], a[0:15]
	s_waitcnt vmcnt(15)
	v_mfma_f32_32x32x16_bf16 a[0:15], v[40:43], v[232:235], a[0:15]
	s_waitcnt vmcnt(13)
	v_mfma_f32_32x32x16_bf16 a[0:15], v[44:47], v[92:95], a[0:15]
	s_waitcnt vmcnt(12)
	v_mfma_f32_32x32x16_bf16 a[0:15], v[44:47], v[140:143], a[0:15]
	s_waitcnt vmcnt(11)
	v_mfma_f32_32x32x16_bf16 a[0:15], v[44:47], v[188:191], a[0:15]
	s_waitcnt vmcnt(10)
	v_mfma_f32_32x32x16_bf16 a[0:15], v[44:47], v[236:239], a[0:15]
	s_waitcnt vmcnt(8)
	v_mfma_f32_32x32x16_bf16 a[0:15], v[48:51], v[96:99], a[0:15]
	s_waitcnt vmcnt(7)
	v_mfma_f32_32x32x16_bf16 a[0:15], v[48:51], v[144:147], a[0:15]
	s_waitcnt vmcnt(6)
	v_mfma_f32_32x32x16_bf16 a[0:15], v[48:51], v[192:195], a[0:15]
	s_waitcnt vmcnt(5)
	v_mfma_f32_32x32x16_bf16 a[0:15], v[48:51], v[240:243], a[0:15]
	v_mul_u32_u24_e32 v1, 0x1080, v1
	s_movk_i32 s4, 0x7f
	s_movk_i32 s6, 0x84
	v_cmp_lt_u32_e32 vcc, s4, v0
	v_lshrrev_b32_e32 v11, 3, v0
	v_and_b32_e32 v10, 31, v0
	v_and_b32_e32 v11, 4, v11
	v_mul_u32_u24_e32 v11, 0x84, v11
	v_lshlrev_b32_e32 v9, 2, v10
	v_bfe_u32 v6, v0, 2, 5
	v_and_b32_e32 v7, 3, v0
	v_add3_u32 v1, v1, v11, v9
	v_lshlrev_b32_e32 v8, 3, v7
	s_waitcnt vmcnt(3)
	v_mfma_f32_32x32x16_bf16 a[0:15], v[52:55], v[100:103], a[0:15]
	s_waitcnt vmcnt(2)
	v_mfma_f32_32x32x16_bf16 a[0:15], v[52:55], v[148:151], a[0:15]
	s_waitcnt vmcnt(1)
	v_mfma_f32_32x32x16_bf16 a[0:15], v[52:55], v[196:199], a[0:15]
	s_waitcnt vmcnt(0)
	v_mfma_f32_32x32x16_bf16 a[0:15], v[52:55], v[244:247], a[0:15]
	s_nop 11
	ds_write_b32 v1, a0
	ds_write_b32 v1, a1 offset:132
	ds_write_b32 v1, a2 offset:264
	ds_write_b32 v1, a3 offset:396
	ds_write_b32 v1, a4 offset:1056
	ds_write_b32 v1, a5 offset:1188
	ds_write_b32 v1, a6 offset:1320
	ds_write_b32 v1, a7 offset:1452
	ds_write_b32 v1, a8 offset:2112
	ds_write_b32 v1, a9 offset:2244
	ds_write_b32 v1, a10 offset:2376
	ds_write_b32 v1, a11 offset:2508
	ds_write_b32 v1, a12 offset:3168
	ds_write_b32 v1, a13 offset:3300
	ds_write_b32 v1, a14 offset:3432
	ds_write_b32 v1, a15 offset:3564
	v_lshlrev_b32_e32 v1, 2, v6
	s_waitcnt lgkmcnt(0)
	s_barrier
	s_and_saveexec_b64 s[4:5], vcc
	s_xor_b64 s[4:5], exec, s[4:5]
	s_cbranch_execz .LBB1_4
	v_mad_u32_u24 v5, v8, s6, v1
	ds_read_b32 v2, v5
	ds_read_b32 v4, v5 offset:4224
	ds_read_b32 v3, v5 offset:8448
	ds_read_b32 v5, v5 offset:12672
	s_waitcnt lgkmcnt(0)
	v_pk_add_f32 v[2:3], v[2:3], v[4:5]
	s_nop 0
	v_add_f32_e32 v3, v2, v3
